# baseline (speedup 1.0000x reference)
_ZN3att10attn64_fwdEPKDF16_S1_S1_PDF16_S2_P15HIP_vector_typeIfLj2EEPiPKfS2_:
	s_load_dwordx2 s[4:5], s[0:1], 0x38
	v_lshl_or_b32 v198, s2, 8, v0
	v_ashrrev_i32_e32 v199, 31, v198
	v_lshlrev_b64 v[2:3], 5, v[198:199]
	s_and_b32 s3, s2, 7
	s_waitcnt lgkmcnt(0)
	v_lshl_add_u64 v[2:3], s[4:5], 0, v[2:3]
	global_load_dwordx4 v[134:137], v[2:3], off offset:16 nt
	global_load_dwordx4 v[130:133], v[2:3], off nt
	s_load_dwordx8 s[8:15], s[0:1], 0x0
	s_load_dwordx8 s[16:23], s[0:1], 0x20
	s_lshr_b32 s4, s2, 4
	s_and_b32 s4, s4, 8
	s_or_b32 s33, s4, s3
	s_bfe_u32 s60, s2, 0x30004
	s_and_b32 s4, s2, 8
	s_waitcnt lgkmcnt(0)
	s_lshr_b32 s22, s2, 8
	s_cmp_lg_u32 s60, 7
	s_cselect_b64 s[24:25], -1, 0
	s_cmp_lg_u32 s4, 0
	s_cbranch_scc0 .LBB1_24
	s_and_b64 vcc, exec, s[24:25]
	s_cbranch_vccz .LBB1_25
	s_xor_b32 s62, s60, 15
	v_readfirstlane_b32 s34, v0
	s_mov_b32 s23, 0
	s_lshr_b32 s63, s34, 6
	s_lshl_b64 s[26:27], s[22:23], 11
	s_lshl_b32 s4, s62, 7
	s_lshl_b32 s31, s33, 19
	s_add_u32 s28, s8, s31
	s_addc_u32 s29, s9, 0
	s_or_b32 s4, s26, s4
	s_lshl_b32 s30, s63, 5
	s_add_u32 s6, s4, s30
	s_addc_u32 s7, s27, 0
	s_lshl_b64 s[4:5], s[6:7], 7
	s_add_u32 s28, s28, s4
	s_addc_u32 s29, s29, s5
	s_lshr_b32 s4, s34, 4
	v_and_b32_e32 v200, 7, v0
	s_and_b32 s4, s4, 4
	v_bfe_u32 v224, v0, 4, 2
	v_bitop3_b32 v216, s4, v200, v224 bitop3:0x36
	s_add_u32 s4, s10, s31
	s_addc_u32 s5, s11, 0
	s_lshl_b64 s[38:39], s[22:23], 18
	s_or_b32 s36, s38, 0x24000
	s_add_u32 s4, s4, s36
	s_addc_u32 s5, s5, s39
	s_lshl_b32 s35, s63, 3
	v_bfe_u32 v1, v0, 3, 3
	v_or_b32_e32 v202, s35, v1
	v_mov_b32_e32 v203, 0
	v_lshlrev_b64 v[2:3], 7, v[202:203]
	v_lshl_add_u64 v[2:3], s[4:5], 0, v[2:3]
	s_add_u32 s4, s12, s31
	s_addc_u32 s5, s13, 0
	s_add_u32 s4, s4, s36
	v_lshlrev_b32_e32 v202, 4, v216
	s_addc_u32 s5, s5, s39
	s_lshl_b32 s36, s63, 4
	v_bfe_u32 v223, v0, 2, 4
	v_lshl_add_u64 v[208:209], v[2:3], 0, v[202:203]
	v_or_b32_e32 v202, s36, v223
	s_lshl_b32 s37, s63, 10
	v_lshlrev_b64 v[2:3], 7, v[202:203]
	v_lshlrev_b32_e32 v4, 3, v0
	s_cmp_lg_u32 0, -1
	v_lshl_add_u64 v[2:3], s[4:5], 0, v[2:3]
	v_and_b32_e32 v202, 24, v4
	s_cselect_b32 s4, 0, 0
	v_lshlrev_b32_e32 v4, 1, v202
	v_mov_b32_e32 v5, v203
	s_add_i32 s65, s37, s4
	s_mov_b32 m0, s65
	s_nop 0
	global_load_lds_dwordx4 v[208:209], off
	s_mov_b64 s[4:5], 0x1000
	v_lshl_add_u64 v[210:211], v[2:3], 0, v[4:5]
	v_lshl_add_u64 v[2:3], v[208:209], 0, s[4:5]
	s_add_i32 s40, s65, 0x1000
	s_mov_b32 m0, s40
	s_nop 0
	global_load_lds_dwordx4 v[2:3], off
	s_add_i32 s66, s65, 0x6000
	s_mov_b32 m0, s66
	s_nop 0
	global_load_lds_dwordx4 v[210:211], off
	s_add_i32 s4, s65, 0x7000
	v_lshl_add_u64 v[2:3], v[210:211], 0, 64
	s_mov_b32 m0, s4
	s_nop 0
	global_load_lds_dwordx4 v[2:3], off
	s_mov_b64 s[4:5], 0x2000
	v_lshl_add_u64 v[2:3], v[208:209], 0, s[4:5]
	s_mov_b64 s[42:43], 0x3000
	v_and_b32_e32 v199, 31, v0
	s_add_i32 s31, s65, 0x2000
	s_mov_b32 m0, s31
	s_nop 0
	global_load_lds_dwordx4 v[2:3], off
	v_lshl_add_u64 v[2:3], v[208:209], 0, s[42:43]
	v_bfe_u32 v201, v0, 5, 1
	s_add_i32 s31, s65, 0x3000
	s_mov_b32 m0, s31
	s_nop 0
	global_load_lds_dwordx4 v[2:3], off
	v_lshlrev_b32_e32 v2, 6, v199
	v_lshl_or_b32 v204, v201, 3, v2
	v_lshlrev_b32_e32 v2, 1, v204
	global_load_dwordx4 v[146:149], v2, s[28:29]
	global_load_dwordx4 v[138:141], v2, s[28:29] offset:32
	global_load_dwordx4 v[122:125], v2, s[28:29] offset:64
	global_load_dwordx4 v[114:117], v2, s[28:29] offset:96
	v_lshrrev_b32_e32 v3, 1, v0
	v_bitop3_b32 v3, v201, v3, 7 bitop3:0x78
	s_mov_b64 s[28:29], 0x4000
	v_lshlrev_b32_e32 v219, 4, v3
	v_mov_b32_e32 v2, v203
	v_mov_b32_e32 v3, v203
	v_mov_b32_e32 v4, v203
	v_mov_b32_e32 v6, v203
	v_mov_b32_e32 v7, v203
	v_mov_b32_e32 v8, v203
	v_mov_b32_e32 v9, v203
	v_mov_b32_e32 v10, v203
	v_mov_b32_e32 v11, v203
	v_mov_b32_e32 v12, v203
	v_mov_b32_e32 v13, v203
	v_mov_b32_e32 v14, v203
	v_mov_b32_e32 v15, v203
	v_mov_b32_e32 v16, v203
	v_mov_b32_e32 v17, v203
	v_lshl_add_u64 v[18:19], v[208:209], 0, s[28:29]
	s_add_i32 s28, s65, 0x4000
	v_lshlrev_b32_e32 v227, 7, v199
	s_mov_b32 m0, s28
	s_nop 0
	global_load_lds_dwordx4 v[18:19], off
	s_mov_b64 s[28:29], 0x5000
	v_add_u32_e32 v231, 0, v227
	v_lshl_add_u64 v[18:19], v[208:209], 0, s[28:29]
	s_add_i32 s28, s65, 0x5000
	s_mov_b32 m0, s28
	s_nop 0
	global_load_lds_dwordx4 v[18:19], off
	s_waitcnt vmcnt(6) lgkmcnt(0)
	s_barrier
	v_add_u32_e32 v232, v231, v219
	ds_read_b128 v[34:37], v232
	ds_read_b128 v[38:41], v232 offset:4096
	v_xor_b32_e32 v220, 32, v219
	s_waitcnt vmcnt(5) lgkmcnt(1)
	v_mfma_f32_32x32x16_f16 v[18:33], v[34:37], v[146:149], v[2:17]
	v_add_u32_e32 v233, v231, v220
	v_xor_b32_e32 v221, 64, v219
	v_add_u32_e32 v234, v231, v221
	v_xor_b32_e32 v222, 0x60, v219
	v_add_u32_e32 v235, v231, v222
	s_cmp_lg_u32 s60, 6
	s_cselect_b64 s[28:29], -1, 0
	s_waitcnt lgkmcnt(0)
	v_mfma_f32_32x32x16_f16 v[2:17], v[38:41], v[146:149], v[2:17]
	ds_read_b128 v[34:37], v233
	ds_read_b128 v[38:41], v233 offset:4096
	s_mov_b32 s31, s23
	v_or_b32_e32 v229, s30, v199
	s_and_b64 vcc, exec, s[28:29]
	v_lshlrev_b32_e32 v230, 2, v201
	s_waitcnt vmcnt(4) lgkmcnt(1)
	v_mfma_f32_32x32x16_f16 v[18:33], v[34:37], v[138:141], v[18:33]
	s_waitcnt lgkmcnt(0)
	v_mfma_f32_32x32x16_f16 v[2:17], v[38:41], v[138:141], v[2:17]
	ds_read_b128 v[34:37], v234
	ds_read_b128 v[38:41], v234 offset:4096
	s_waitcnt vmcnt(3) lgkmcnt(1)
	v_mfma_f32_32x32x16_f16 v[18:33], v[34:37], v[122:125], v[18:33]
	s_waitcnt lgkmcnt(0)
	v_mfma_f32_32x32x16_f16 v[2:17], v[38:41], v[122:125], v[2:17]
	ds_read_b128 v[34:37], v235
	ds_read_b128 v[38:41], v235 offset:4096
	s_waitcnt vmcnt(0) lgkmcnt(1)
	v_mfma_f32_32x32x16_f16 v[18:33], v[34:37], v[114:117], v[18:33]
	s_waitcnt lgkmcnt(0)
	v_mfma_f32_32x32x16_f16 v[2:17], v[38:41], v[114:117], v[2:17]
	s_cbranch_vccnz .LBB1_4
	v_or_b32_e32 v34, 32, v230
	v_mov_b32_e32 v35, 0xff800000
	v_cmp_le_u32_e32 vcc, v34, v229
	v_or_b32_e32 v34, 33, v230
	s_nop 6
	v_cndmask_b32_e32 v2, v35, v2, vcc
	v_cmp_lt_u32_e32 vcc, v230, v229
	s_nop 1
	v_cndmask_b32_e32 v19, v35, v19, vcc
	v_cmp_le_u32_e32 vcc, v230, v229
	s_nop 1
	v_cndmask_b32_e32 v18, v35, v18, vcc
	v_cmp_le_u32_e32 vcc, v34, v229
	v_or_b32_e32 v34, 2, v230
	s_nop 0
	v_cndmask_b32_e32 v3, v35, v3, vcc
	v_cmp_le_u32_e32 vcc, v34, v229
	v_or_b32_e32 v34, 34, v230
	s_nop 0
	v_cndmask_b32_e32 v20, v35, v20, vcc
	v_cmp_le_u32_e32 vcc, v34, v229
	v_or_b32_e32 v34, 3, v230
	s_nop 0
	v_cndmask_b32_e32 v4, v35, v4, vcc
	v_cmp_le_u32_e32 vcc, v34, v229
	v_or_b32_e32 v34, 35, v230
	s_nop 0
	v_cndmask_b32_e32 v21, v35, v21, vcc
	v_cmp_le_u32_e32 vcc, v34, v229
	v_or_b32_e32 v34, 8, v230
	s_nop 0
	v_cndmask_b32_e32 v5, v35, v5, vcc
	v_cmp_le_u32_e32 vcc, v34, v229
	v_or_b32_e32 v34, 40, v230
	s_nop 0
	v_cndmask_b32_e32 v22, v35, v22, vcc
	v_cmp_le_u32_e32 vcc, v34, v229
	v_or_b32_e32 v34, 9, v230
	s_nop 0
	v_cndmask_b32_e32 v6, v35, v6, vcc
	v_cmp_le_u32_e32 vcc, v34, v229
	v_or_b32_e32 v34, 41, v230
	s_nop 0
	v_cndmask_b32_e32 v23, v35, v23, vcc
	v_cmp_le_u32_e32 vcc, v34, v229
	v_or_b32_e32 v34, 10, v230
	s_nop 0
	v_cndmask_b32_e32 v7, v35, v7, vcc
	v_cmp_le_u32_e32 vcc, v34, v229
	v_or_b32_e32 v34, 42, v230
	s_nop 0
	v_cndmask_b32_e32 v24, v35, v24, vcc
	v_cmp_le_u32_e32 vcc, v34, v229
	v_or_b32_e32 v34, 11, v230
	s_nop 0
	v_cndmask_b32_e32 v8, v35, v8, vcc
	v_cmp_le_u32_e32 vcc, v34, v229
	v_or_b32_e32 v34, 43, v230
	s_nop 0
	v_cndmask_b32_e32 v25, v35, v25, vcc
	v_cmp_le_u32_e32 vcc, v34, v229
	v_or_b32_e32 v34, 16, v230
	s_nop 0
	v_cndmask_b32_e32 v9, v35, v9, vcc
	v_cmp_le_u32_e32 vcc, v34, v229
	v_or_b32_e32 v34, 48, v230
	s_nop 0
	v_cndmask_b32_e32 v26, v35, v26, vcc
	v_cmp_le_u32_e32 vcc, v34, v229
	v_or_b32_e32 v34, 17, v230
	s_nop 0
	v_cndmask_b32_e32 v10, v35, v10, vcc
	v_cmp_le_u32_e32 vcc, v34, v229
	v_or_b32_e32 v34, 49, v230
	s_nop 0
	v_cndmask_b32_e32 v27, v35, v27, vcc
	v_cmp_le_u32_e32 vcc, v34, v229
	v_or_b32_e32 v34, 18, v230
	s_nop 0
	v_cndmask_b32_e32 v11, v35, v11, vcc
	v_cmp_le_u32_e32 vcc, v34, v229
	v_or_b32_e32 v34, 50, v230
	s_nop 0
	v_cndmask_b32_e32 v28, v35, v28, vcc
	v_cmp_le_u32_e32 vcc, v34, v229
	v_or_b32_e32 v34, 19, v230
	s_nop 0
	v_cndmask_b32_e32 v12, v35, v12, vcc
	v_cmp_le_u32_e32 vcc, v34, v229
	v_or_b32_e32 v34, 51, v230
	s_nop 0
	v_cndmask_b32_e32 v29, v35, v29, vcc
	v_cmp_le_u32_e32 vcc, v34, v229
	v_or_b32_e32 v34, 24, v230
	s_nop 0
	v_cndmask_b32_e32 v13, v35, v13, vcc
	v_cmp_le_u32_e32 vcc, v34, v229
	v_or_b32_e32 v34, 56, v230
	s_nop 0
	v_cndmask_b32_e32 v30, v35, v30, vcc
	v_cmp_le_u32_e32 vcc, v34, v229
	v_or_b32_e32 v34, 25, v230
	s_nop 0
	v_cndmask_b32_e32 v14, v35, v14, vcc
	v_cmp_le_u32_e32 vcc, v34, v229
	v_or_b32_e32 v34, 57, v230
	s_nop 0
	v_cndmask_b32_e32 v31, v35, v31, vcc
	v_cmp_le_u32_e32 vcc, v34, v229
	v_or_b32_e32 v34, 26, v230
	s_nop 0
	v_cndmask_b32_e32 v15, v35, v15, vcc
	v_cmp_le_u32_e32 vcc, v34, v229
	v_or_b32_e32 v34, 58, v230
	s_nop 0
	v_cndmask_b32_e32 v32, v35, v32, vcc
	v_cmp_le_u32_e32 vcc, v34, v229
	v_or_b32_e32 v34, 27, v230
	s_nop 0
	v_cndmask_b32_e32 v16, v35, v16, vcc
	v_cmp_le_u32_e32 vcc, v34, v229
	v_or_b32_e32 v34, 59, v230
	s_nop 0
	v_cndmask_b32_e32 v33, v35, v33, vcc
	v_cmp_le_u32_e32 vcc, v34, v229
	s_nop 1
	v_cndmask_b32_e32 v17, v35, v17, vcc

.LBB1_97:
	v_readfirstlane_b32 s36, v0
	s_lshr_b32 s23, s36, 6
	s_lshl_b32 s4, s60, 7
	s_lshl_b64 s[28:29], s[28:29], 1
	s_add_u32 s30, s8, s28
	s_addc_u32 s31, s9, s29
	s_or_b32 s4, s26, s4
	s_lshl_b32 s39, s23, 5
	s_add_u32 s6, s4, s39
	s_addc_u32 s7, s27, 0
	s_lshl_b64 s[4:5], s[6:7], 7
	s_add_u32 s30, s30, s4
	s_addc_u32 s31, s31, s5
	s_lshr_b32 s4, s36, 4
	s_and_b32 s4, s4, 4
	v_bitop3_b32 v190, s4, v200, v224 bitop3:0x36
	s_add_u32 s4, s10, s28
	s_addc_u32 s5, s11, s29
	s_lshl_b64 s[26:27], s[34:35], 1
	s_add_u32 s4, s4, s26
	s_addc_u32 s5, s5, s27
	s_lshl_b32 s35, s23, 3
	v_or_b32_e32 v2, s35, v1
	v_mov_b32_e32 v3, 0
	v_lshlrev_b64 v[4:5], 7, v[2:3]
	v_lshl_add_u64 v[4:5], s[4:5], 0, v[4:5]
	s_add_u32 s4, s12, s28
	s_addc_u32 s5, s13, s29
	s_add_u32 s4, s4, s26
	v_lshlrev_b32_e32 v2, 3, v190
	s_addc_u32 s5, s5, s27
	s_lshl_b32 s37, s23, 4
	v_lshl_add_u64 v[50:51], v[2:3], 1, v[4:5]
	v_or_b32_e32 v2, s37, v223
	s_lshl_b32 s34, s23, 10
	v_lshlrev_b64 v[4:5], 7, v[2:3]
	s_cmp_lg_u32 0, -1
	v_lshl_add_u64 v[4:5], s[4:5], 0, v[4:5]
	s_cselect_b32 s4, 0, 0
	s_add_i32 s59, s34, s4
	s_mov_b32 m0, s59
	s_nop 0
	global_load_lds_dwordx4 v[50:51], off
	s_mov_b64 s[4:5], 0x1000
	v_lshl_add_u64 v[52:53], v[202:203], 1, v[4:5]
	v_lshl_add_u64 v[4:5], v[50:51], 0, s[4:5]
	s_add_i32 s38, s59, 0x1000
	s_mov_b32 m0, s38
	s_nop 0
	global_load_lds_dwordx4 v[4:5], off
	s_add_i32 s62, s59, 0x6000
	s_mov_b32 m0, s62
	s_nop 0
	global_load_lds_dwordx4 v[52:53], off
	s_add_i32 s4, s59, 0x7000
	v_lshl_add_u64 v[4:5], v[52:53], 0, 64
	s_mov_b32 m0, s4
	s_nop 0
	global_load_lds_dwordx4 v[4:5], off
	s_mov_b64 s[4:5], 0x2000
	s_add_i32 s40, s59, 0x2000
	v_lshl_add_u64 v[4:5], v[50:51], 0, s[4:5]
	s_mov_b32 m0, s40
	s_nop 0
	global_load_lds_dwordx4 v[4:5], off
	s_mov_b64 s[40:41], 0x3000
	v_lshl_add_u64 v[4:5], v[50:51], 0, s[40:41]
	s_add_i32 s40, s59, 0x3000
	s_mov_b32 m0, s40
	s_nop 0
	global_load_lds_dwordx4 v[4:5], off
	v_lshl_add_u64 v[12:13], v[204:205], 1, s[30:31]
	global_load_dwordx4 v[146:149], v[12:13], off
	global_load_dwordx4 v[138:141], v[12:13], off offset:32
	global_load_dwordx4 v[118:121], v[12:13], off offset:64
	global_load_dwordx4 v[114:117], v[12:13], off offset:96
	s_mov_b64 s[30:31], 0x4000
	v_mov_b32_e32 v4, v3
	v_mov_b32_e32 v5, v3
	v_mov_b32_e32 v6, v3
	v_mov_b32_e32 v7, v3
	v_mov_b32_e32 v8, v3
	v_mov_b32_e32 v9, v3
	v_mov_b32_e32 v10, v3
	v_mov_b32_e32 v11, v3
	v_mov_b32_e32 v12, v3
	v_mov_b32_e32 v13, v3
	v_mov_b32_e32 v14, v3
	v_mov_b32_e32 v15, v3
	v_mov_b32_e32 v16, v3
	v_mov_b32_e32 v17, v3
	v_mov_b32_e32 v2, v3
	s_mov_b64 s[40:41], 0x5000
	v_lshl_add_u64 v[18:19], v[50:51], 0, s[30:31]
	s_add_i32 s30, s59, 0x4000
	s_mov_b32 m0, s30
	s_nop 0
	global_load_lds_dwordx4 v[18:19], off
	v_add_u32_e32 v217, 0, v227
	v_lshl_add_u64 v[20:21], v[50:51], 0, s[40:41]
	s_add_i32 s31, s59, 0x5000
	s_mov_b32 m0, s31
	s_nop 0
	global_load_lds_dwordx4 v[20:21], off
	v_add_u32_e32 v224, v217, v219
	s_waitcnt vmcnt(6) lgkmcnt(0)
	s_barrier
	ds_read_b128 v[34:37], v224
	ds_read_b128 v[38:41], v224 offset:4096
	v_add_u32_e32 v227, v217, v220
	v_add_u32_e32 v229, v217, v221
	v_add_u32_e32 v230, v217, v222
	s_cmp_lg_u32 s60, 0
	s_cselect_b64 s[30:31], -1, 0
	v_or_b32_e32 v214, s39, v199
	s_and_b64 vcc, exec, s[30:31]
	v_lshlrev_b32_e32 v215, 2, v201
	s_waitcnt vmcnt(5) lgkmcnt(1)
	v_mfma_f32_32x32x16_f16 v[18:33], v[34:37], v[146:149], v[2:17]
	s_waitcnt lgkmcnt(0)
	v_mfma_f32_32x32x16_f16 v[2:17], v[38:41], v[146:149], v[2:17]
	ds_read_b128 v[34:37], v227
	ds_read_b128 v[38:41], v227 offset:4096
	s_waitcnt vmcnt(4) lgkmcnt(1)
	v_mfma_f32_32x32x16_f16 v[18:33], v[34:37], v[138:141], v[18:33]
	s_waitcnt lgkmcnt(0)
	v_mfma_f32_32x32x16_f16 v[2:17], v[38:41], v[138:141], v[2:17]
	ds_read_b128 v[34:37], v229
	ds_read_b128 v[38:41], v229 offset:4096
	s_waitcnt vmcnt(3) lgkmcnt(1)
	v_mfma_f32_32x32x16_f16 v[18:33], v[34:37], v[118:121], v[18:33]
	s_waitcnt lgkmcnt(0)
	v_mfma_f32_32x32x16_f16 v[2:17], v[38:41], v[118:121], v[2:17]
	ds_read_b128 v[34:37], v230
	ds_read_b128 v[38:41], v230 offset:4096
	s_waitcnt vmcnt(0) lgkmcnt(1)
	v_mfma_f32_32x32x16_f16 v[18:33], v[34:37], v[114:117], v[18:33]
	s_waitcnt lgkmcnt(0)
	v_mfma_f32_32x32x16_f16 v[2:17], v[38:41], v[114:117], v[2:17]
	s_cbranch_vccnz .LBB1_99
	v_or_b32_e32 v34, 32, v215
	v_mov_b32_e32 v35, 0xff800000
	v_cmp_le_u32_e32 vcc, v34, v214
	v_or_b32_e32 v34, 33, v215
	s_nop 6
	v_cndmask_b32_e32 v2, v35, v2, vcc
	v_cmp_lt_u32_e32 vcc, v215, v214
	s_nop 1
	v_cndmask_b32_e32 v19, v35, v19, vcc
	v_cmp_le_u32_e32 vcc, v215, v214
	s_nop 1
	v_cndmask_b32_e32 v18, v35, v18, vcc
	v_cmp_le_u32_e32 vcc, v34, v214
	v_or_b32_e32 v34, 2, v215
	s_nop 0
	v_cndmask_b32_e32 v3, v35, v3, vcc
	v_cmp_le_u32_e32 vcc, v34, v214
	v_or_b32_e32 v34, 34, v215
	s_nop 0
	v_cndmask_b32_e32 v20, v35, v20, vcc
	v_cmp_le_u32_e32 vcc, v34, v214
	v_or_b32_e32 v34, 3, v215
	s_nop 0
	v_cndmask_b32_e32 v4, v35, v4, vcc
	v_cmp_le_u32_e32 vcc, v34, v214
	v_or_b32_e32 v34, 35, v215
	s_nop 0
	v_cndmask_b32_e32 v21, v35, v21, vcc
	v_cmp_le_u32_e32 vcc, v34, v214
	v_or_b32_e32 v34, 8, v215
	s_nop 0
	v_cndmask_b32_e32 v5, v35, v5, vcc
	v_cmp_le_u32_e32 vcc, v34, v214
	v_or_b32_e32 v34, 40, v215
	s_nop 0
	v_cndmask_b32_e32 v22, v35, v22, vcc
	v_cmp_le_u32_e32 vcc, v34, v214
	v_or_b32_e32 v34, 9, v215
	s_nop 0
	v_cndmask_b32_e32 v6, v35, v6, vcc
	v_cmp_le_u32_e32 vcc, v34, v214
	v_or_b32_e32 v34, 41, v215
	s_nop 0
	v_cndmask_b32_e32 v23, v35, v23, vcc
	v_cmp_le_u32_e32 vcc, v34, v214
	v_or_b32_e32 v34, 10, v215
	s_nop 0
	v_cndmask_b32_e32 v7, v35, v7, vcc
	v_cmp_le_u32_e32 vcc, v34, v214
	v_or_b32_e32 v34, 42, v215
	s_nop 0
	v_cndmask_b32_e32 v24, v35, v24, vcc
	v_cmp_le_u32_e32 vcc, v34, v214
	v_or_b32_e32 v34, 11, v215
	s_nop 0
	v_cndmask_b32_e32 v8, v35, v8, vcc
	v_cmp_le_u32_e32 vcc, v34, v214
	v_or_b32_e32 v34, 43, v215
	s_nop 0
	v_cndmask_b32_e32 v25, v35, v25, vcc
	v_cmp_le_u32_e32 vcc, v34, v214
	v_or_b32_e32 v34, 16, v215
	s_nop 0
	v_cndmask_b32_e32 v9, v35, v9, vcc
	v_cmp_le_u32_e32 vcc, v34, v214
	v_or_b32_e32 v34, 48, v215
	s_nop 0
	v_cndmask_b32_e32 v26, v35, v26, vcc
	v_cmp_le_u32_e32 vcc, v34, v214
	v_or_b32_e32 v34, 17, v215
	s_nop 0
	v_cndmask_b32_e32 v10, v35, v10, vcc
	v_cmp_le_u32_e32 vcc, v34, v214
	v_or_b32_e32 v34, 49, v215
	s_nop 0
	v_cndmask_b32_e32 v27, v35, v27, vcc
	v_cmp_le_u32_e32 vcc, v34, v214
	v_or_b32_e32 v34, 18, v215
	s_nop 0
	v_cndmask_b32_e32 v11, v35, v11, vcc
	v_cmp_le_u32_e32 vcc, v34, v214
	v_or_b32_e32 v34, 50, v215
	s_nop 0
	v_cndmask_b32_e32 v28, v35, v28, vcc
	v_cmp_le_u32_e32 vcc, v34, v214
	v_or_b32_e32 v34, 19, v215
	s_nop 0
	v_cndmask_b32_e32 v12, v35, v12, vcc
	v_cmp_le_u32_e32 vcc, v34, v214
	v_or_b32_e32 v34, 51, v215
	s_nop 0
	v_cndmask_b32_e32 v29, v35, v29, vcc
	v_cmp_le_u32_e32 vcc, v34, v214
	v_or_b32_e32 v34, 24, v215
	s_nop 0
	v_cndmask_b32_e32 v13, v35, v13, vcc
	v_cmp_le_u32_e32 vcc, v34, v214
	v_or_b32_e32 v34, 56, v215
	s_nop 0
	v_cndmask_b32_e32 v30, v35, v30, vcc
	v_cmp_le_u32_e32 vcc, v34, v214
	v_or_b32_e32 v34, 25, v215
	s_nop 0
	v_cndmask_b32_e32 v14, v35, v14, vcc
	v_cmp_le_u32_e32 vcc, v34, v214
	v_or_b32_e32 v34, 57, v215
	s_nop 0
	v_cndmask_b32_e32 v31, v35, v31, vcc
	v_cmp_le_u32_e32 vcc, v34, v214
	v_or_b32_e32 v34, 26, v215
	s_nop 0
	v_cndmask_b32_e32 v15, v35, v15, vcc
	v_cmp_le_u32_e32 vcc, v34, v214
	v_or_b32_e32 v34, 58, v215
	s_nop 0
	v_cndmask_b32_e32 v32, v35, v32, vcc
	v_cmp_le_u32_e32 vcc, v34, v214
	v_or_b32_e32 v34, 27, v215
	s_nop 0
	v_cndmask_b32_e32 v16, v35, v16, vcc
	v_cmp_le_u32_e32 vcc, v34, v214
	v_or_b32_e32 v34, 59, v215
	s_nop 0
	v_cndmask_b32_e32 v33, v35, v33, vcc
	v_cmp_le_u32_e32 vcc, v34, v214
	s_nop 1
	v_cndmask_b32_e32 v17, v35, v17, vcc

.LBB1_127:
	v_bfe_u32 v210, v0, 5, 1
	s_and_b64 vcc, exec, s[24:25]
	v_bfe_u32 v220, v0, 4, 2
	v_bfe_u32 v199, v0, 3, 3
	v_bfe_u32 v218, v0, 2, 4
	v_and_b32_e32 v201, 63, v0
	v_and_b32_e32 v211, 31, v0
	v_and_b32_e32 v1, 7, v0
	v_lshrrev_b32_e32 v217, 1, v0
	v_lshlrev_b32_e32 v219, 3, v0
	v_lshlrev_b32_e32 v215, 1, v0
	v_lshlrev_b32_e32 v214, 8, v210
	v_lshlrev_b32_e32 v216, 4, v0
	v_lshlrev_b32_e32 v212, 4, v210
	v_and_b32_e32 v213, 3, v0
	s_cbranch_vccz .LBB1_193
	s_xor_b32 s52, s60, 15
	v_readfirstlane_b32 s7, v0
	s_mov_b32 s23, 0
	s_lshr_b32 s53, s7, 6
	s_lshl_b64 s[0:1], s[22:23], 11
	s_lshl_b32 s6, s52, 7
	s_lshl_b32 s50, s33, 18
	s_lshl_b32 s28, s33, 19
	s_add_u32 s26, s8, s28
	s_addc_u32 s27, s9, 0
	s_or_b32 s0, s0, s6
	s_lshl_b32 s6, s53, 5
	s_add_u32 s0, s0, s6
	s_addc_u32 s1, s1, 0
	s_lshl_b64 s[24:25], s[0:1], 6
	s_lshl_b64 s[0:1], s[0:1], 7
	s_add_u32 s26, s26, s0
	s_addc_u32 s27, s27, s1
	s_lshr_b32 s0, s7, 4
	s_and_b32 s31, s7, 0x3fffffc0
	v_and_b32_e32 v200, 7, v0
	s_and_b32 s0, s0, 4
	v_bitop3_b32 v4, s0, v200, v220 bitop3:0x36
	s_add_u32 s0, s10, s28
	s_addc_u32 s1, s11, 0
	s_lshl_b64 s[34:35], s[22:23], 18
	s_add_u32 s0, s0, s34
	v_lshl_or_b32 v194, s53, 3, v199
	v_mov_b32_e32 v195, 0
	s_addc_u32 s1, s1, s35
	v_lshlrev_b64 v[86:87], 7, v[194:195]
	v_lshl_add_u64 v[2:3], s[0:1], 0, v[86:87]
	s_add_u32 s0, s12, s28
	s_addc_u32 s1, s13, 0
	v_lshlrev_b32_e32 v194, 4, v4
	s_add_u32 s0, s0, s34
	v_lshl_add_u64 v[206:207], v[2:3], 0, v[194:195]
	s_addc_u32 s1, s1, s35
	v_lshl_or_b32 v2, s53, 4, v218
	v_mov_b32_e32 v3, v195
	s_lshl_b32 s54, s53, 10
	v_lshlrev_b64 v[88:89], 7, v[2:3]
	s_cmp_lg_u32 0, -1
	v_lshl_add_u64 v[2:3], s[0:1], 0, v[88:89]
	v_and_b32_e32 v10, 24, v219
	s_cselect_b32 s0, 0, 0
	v_lshlrev_b32_e32 v4, 1, v10
	v_mov_b32_e32 v5, v195
	s_add_i32 s56, s54, s0
	s_mov_b32 m0, s56
	s_nop 0
	global_load_lds_dwordx4 v[206:207], off
	s_mov_b64 s[0:1], 0x1000
	v_lshl_add_u64 v[204:205], v[2:3], 0, v[4:5]
	v_lshl_add_u64 v[2:3], v[206:207], 0, s[0:1]
	s_add_i32 s30, s56, 0x1000
	s_mov_b32 m0, s30
	s_nop 0
	global_load_lds_dwordx4 v[2:3], off
	s_add_i32 s55, s56, 0x6000
	s_mov_b32 m0, s55
	s_nop 0
	global_load_lds_dwordx4 v[204:205], off
	s_add_i32 s0, s56, 0x7000
	v_lshl_add_u64 v[2:3], v[204:205], 0, 64
	s_mov_b32 m0, s0
	s_nop 0
	global_load_lds_dwordx4 v[2:3], off
	s_mov_b64 s[0:1], 0x2000
	v_lshl_add_u64 v[2:3], v[206:207], 0, s[0:1]
	s_mov_b64 s[28:29], 0x3000
	v_lshlrev_b32_e32 v4, 7, v211
	s_add_i32 s7, s56, 0x2000
	s_mov_b32 m0, s7
	s_nop 0
	global_load_lds_dwordx4 v[2:3], off
	v_lshl_add_u64 v[2:3], v[206:207], 0, s[28:29]
	s_add_i32 s7, s56, 0x3000
	s_mov_b32 m0, s7
	s_nop 0
	global_load_lds_dwordx4 v[2:3], off
	v_or_b32_e32 v2, v212, v4
	global_load_dwordx4 v[166:169], v2, s[26:27]
	global_load_dwordx4 v[162:165], v2, s[26:27] offset:32
	global_load_dwordx4 v[154:157], v2, s[26:27] offset:64
	global_load_dwordx4 v[146:149], v2, s[26:27] offset:96
	v_bitop3_b32 v3, v210, v217, 7 bitop3:0x78
	v_mov_b32_e32 v18, v195
	v_mov_b32_e32 v19, v195
	v_mov_b32_e32 v20, v195
	v_mov_b32_e32 v21, v195
	v_mov_b32_e32 v22, v195
	v_mov_b32_e32 v23, v195
	v_mov_b32_e32 v24, v195
	v_mov_b32_e32 v25, v195
	v_mov_b32_e32 v26, v195
	v_mov_b32_e32 v27, v195
	v_mov_b32_e32 v28, v195
	v_mov_b32_e32 v29, v195
	v_mov_b32_e32 v30, v195
	v_mov_b32_e32 v31, v195
	v_mov_b32_e32 v32, v195
	v_mov_b32_e32 v33, v195
	s_mov_b64 s[26:27], 0x4000
	v_lshlrev_b32_e32 v226, 4, v3
	v_lshl_add_u64 v[2:3], v[206:207], 0, s[26:27]
	s_add_i32 s7, s56, 0x4000
	s_mov_b32 m0, s7
	s_nop 0
	global_load_lds_dwordx4 v[2:3], off
	s_mov_b64 s[28:29], 0x5000
	v_add_u32_e32 v227, 0, v4
	v_lshl_add_u64 v[2:3], v[206:207], 0, s[28:29]
	s_add_i32 s7, s56, 0x5000
	s_mov_b32 m0, s7
	s_nop 0
	global_load_lds_dwordx4 v[2:3], off
	s_waitcnt vmcnt(6) lgkmcnt(0)
	s_barrier
	v_add_u32_e32 v225, v227, v226
	ds_read_b128 v[2:5], v225
	ds_read_b128 v[6:9], v225 offset:4096
	v_xor_b32_e32 v228, 32, v226
	v_add_u32_e32 v224, v227, v228
	s_waitcnt vmcnt(5) lgkmcnt(0)
	v_mfma_f32_32x32x16_f16 v[34:49], v[2:5], v[166:169], v[18:33]
	v_xor_b32_e32 v229, 64, v226
	v_add_u32_e32 v223, v227, v229
	v_xor_b32_e32 v230, 0x60, v226
	v_add_u32_e32 v222, v227, v230
	v_and_b32_e32 v11, 32, v215
	s_lshl_b32 s28, s31, 2
	s_add_i32 s51, s28, 0
	v_mfma_f32_32x32x16_f16 v[18:33], v[6:9], v[166:169], v[18:33]
	ds_read_b128 v[2:5], v224
	ds_read_b128 v[6:9], v224 offset:4096
	s_mov_b64 s[28:29], 0x6000
	s_mov_b64 s[36:37], 0x7000
	s_lshl_b32 s31, s2, 15
	s_and_b32 s31, s31, 0x400000
	s_mov_b32 s7, s23
	s_mov_b32 s57, -1
	s_waitcnt vmcnt(4) lgkmcnt(1)
	v_mfma_f32_32x32x16_f16 v[34:49], v[2:5], v[162:165], v[34:49]
	s_movk_i32 s60, 0x2000
	s_movk_i32 s58, 0x4000
	v_lshl_add_u32 v221, v211, 2, s51
	s_mov_b64 s[38:39], 0x4040
	s_mov_b32 s59, 0x41000000
	s_mov_b64 s[40:41], 0xa000
	s_mov_b64 s[42:43], 0xb000
	s_waitcnt lgkmcnt(0)
	v_mfma_f32_32x32x16_f16 v[18:33], v[6:9], v[162:165], v[18:33]
	ds_read_b128 v[2:5], v223
	ds_read_b128 v[6:9], v223 offset:4096
	s_mov_b64 s[44:45], 0x6040
	s_waitcnt vmcnt(3) lgkmcnt(1)
	v_mfma_f32_32x32x16_f16 v[34:49], v[2:5], v[154:157], v[34:49]
	ds_read_b128 v[2:5], v222
	s_waitcnt lgkmcnt(1)
	v_mfma_f32_32x32x16_f16 v[18:33], v[6:9], v[154:157], v[18:33]
	ds_read_b128 v[6:9], v222 offset:4096
	s_waitcnt vmcnt(0) lgkmcnt(1)
	v_mfma_f32_32x32x16_f16 v[34:49], v[2:5], v[146:149], v[34:49]
	v_add3_u32 v2, 0, v11, v10
	v_and_b32_e32 v3, 0xc0, v216
	v_add3_u32 v203, v2, v214, v3
	s_waitcnt lgkmcnt(0)
	v_mfma_f32_32x32x16_f16 v[18:33], v[6:9], v[146:149], v[18:33]
	s_nop 6
	v_max_f32_e32 v2, v35, v35
	v_max_f32_e32 v3, v34, v34
	v_max_f32_e32 v2, v3, v2
	s_nop 1
	v_max3_f32 v3, v36, v37, v19
	v_max3_f32 v2, v2, v18, v20
	v_max3_f32 v2, v2, v21, v38
	v_max3_f32 v3, v3, v40, v41
	v_max3_f32 v2, v2, v39, v22
	v_max3_f32 v3, v3, v24, v25
	v_max3_f32 v2, v2, v23, v42
	v_max3_f32 v3, v3, v44, v45
	v_max3_f32 v2, v2, v43, v26
	v_max3_f32 v3, v3, v28, v29
	v_max3_f32 v2, v2, v27, v46
	v_max3_f32 v3, v3, v48, v49
	v_max3_f32 v2, v2, v47, v30
	v_max3_f32 v3, v3, v32, v33
	v_max3_f32 v2, v2, v31, v3
	v_mov_b32_e32 v3, v2
	s_nop 1
	v_permlane32_swap_b32_e32 v2, v3
	v_max_f32_e32 v3, v3, v3
	v_max_f32_e32 v2, v2, v2
	v_max_f32_e32 v202, v2, v3
	v_sub_f32_e32 v18, v18, v202
	v_exp_f32_e32 v50, v18
	v_sub_f32_e32 v18, v35, v202
	v_exp_f32_e32 v67, v18
	v_sub_f32_e32 v18, v19, v202
	v_exp_f32_e32 v51, v18
	v_sub_f32_e32 v18, v36, v202
	v_exp_f32_e32 v68, v18
	v_sub_f32_e32 v18, v20, v202
	v_exp_f32_e32 v52, v18
	v_sub_f32_e32 v18, v37, v202
	v_exp_f32_e32 v69, v18
	v_sub_f32_e32 v18, v21, v202
	v_exp_f32_e32 v53, v18
	v_sub_f32_e32 v18, v38, v202
	v_exp_f32_e32 v70, v18
	v_sub_f32_e32 v18, v22, v202
	v_exp_f32_e32 v54, v18
	v_sub_f32_e32 v18, v39, v202
	v_exp_f32_e32 v71, v18
	v_sub_f32_e32 v18, v23, v202
	v_exp_f32_e32 v55, v18
	v_sub_f32_e32 v18, v40, v202
	v_exp_f32_e32 v72, v18
	v_sub_f32_e32 v18, v24, v202
	v_exp_f32_e32 v56, v18
	v_sub_f32_e32 v18, v41, v202
	v_exp_f32_e32 v73, v18
	v_sub_f32_e32 v18, v25, v202
	v_exp_f32_e32 v57, v18
	v_sub_f32_e32 v18, v42, v202
	v_exp_f32_e32 v74, v18
	v_sub_f32_e32 v18, v26, v202
	v_exp_f32_e32 v58, v18
	v_sub_f32_e32 v18, v43, v202
	v_exp_f32_e32 v75, v18
	v_sub_f32_e32 v18, v27, v202
	v_exp_f32_e32 v59, v18
	v_sub_f32_e32 v18, v44, v202
	v_exp_f32_e32 v76, v18
	v_sub_f32_e32 v18, v28, v202
	v_exp_f32_e32 v60, v18
	v_sub_f32_e32 v18, v45, v202
	v_exp_f32_e32 v77, v18
	v_sub_f32_e32 v18, v29, v202
	v_exp_f32_e32 v61, v18
	v_sub_f32_e32 v18, v46, v202
	v_exp_f32_e32 v78, v18
	v_sub_f32_e32 v18, v30, v202
	v_exp_f32_e32 v62, v18
	v_sub_f32_e32 v18, v47, v202
	v_exp_f32_e32 v79, v18
	v_sub_f32_e32 v18, v31, v202
	v_exp_f32_e32 v63, v18
	v_sub_f32_e32 v18, v48, v202
	v_exp_f32_e32 v80, v18
	v_sub_f32_e32 v18, v32, v202
	v_xor_b32_e32 v2, 0x80000000, v202
	v_exp_f32_e32 v64, v18
	v_sub_f32_e32 v18, v49, v202
	v_mov_b32_e32 v3, v2
	v_mov_b32_e32 v4, v2
	v_mov_b32_e32 v5, v2
	v_mov_b32_e32 v6, v2
	v_mov_b32_e32 v7, v2
	v_mov_b32_e32 v8, v2
	v_mov_b32_e32 v9, v2
	v_mov_b32_e32 v10, v2
	v_mov_b32_e32 v11, v2
	v_mov_b32_e32 v12, v2
	v_mov_b32_e32 v13, v2
	v_mov_b32_e32 v14, v2
	v_mov_b32_e32 v15, v2
	v_mov_b32_e32 v16, v2
	v_mov_b32_e32 v17, v2
	v_exp_f32_e32 v81, v18
	v_sub_f32_e32 v18, v33, v202
	v_exp_f32_e32 v65, v18
	s_waitcnt vmcnt(0) lgkmcnt(0)
	s_barrier
	v_lshl_add_u64 v[18:19], v[206:207], 0, s[28:29]
	s_mov_b32 m0, s56
	s_nop 0
	global_load_lds_dwordx4 v[18:19], off
	v_lshl_add_u64 v[18:19], v[206:207], 0, s[36:37]
	s_mov_b32 m0, s30
	s_nop 0
	global_load_lds_dwordx4 v[18:19], off
	v_lshl_add_u64 v[18:19], v[204:205], 0, s[0:1]
	s_add_i32 s0, s56, 0x8000
	s_mov_b32 m0, s0
	s_nop 0
	global_load_lds_dwordx4 v[18:19], off
	s_mov_b64 s[0:1], 0x2040
	v_lshl_add_u64 v[18:19], v[204:205], 0, s[0:1]
	s_add_i32 s0, s56, 0x9000
	s_mov_b32 m0, s0
	s_nop 0
	global_load_lds_dwordx4 v[18:19], off
	ds_read_b128 v[82:85], v225 offset:8192
	ds_read_b128 v[178:181], v225 offset:12288
	ds_read_b128 v[174:177], v224 offset:8192
	ds_read_b128 v[170:173], v224 offset:12288
	ds_read_b128 v[126:129], v223 offset:8192
	ds_read_b128 v[122:125], v223 offset:12288
	ds_read_b128 v[118:121], v222 offset:8192
	ds_read_b128 v[114:117], v222 offset:12288
	v_sub_f32_e32 v34, v34, v202
	v_lshl_add_u64 v[18:19], s[34:35], 0, v[88:89]
	v_exp_f32_e32 v66, v34
	v_lshl_or_b32 v18, v213, 4, v18
	s_waitcnt vmcnt(4) lgkmcnt(0)
	s_barrier
	v_lshl_add_u64 v[190:191], s[12:13], 0, v[18:19]
	v_lshl_add_u64 v[18:19], s[34:35], 0, v[86:87]
	s_lshl_b32 s30, s3, 19
	v_or_b32_e32 v18, v18, v194
	v_cmp_gt_u32_e64 s[0:1], 32, v201
	s_or_b32 s30, s31, s30
	s_mov_b32 s31, s23
	v_lshl_add_u64 v[192:193], s[10:11], 0, v[18:19]
	s_mov_b64 s[34:35], 0x8000
	s_mov_b64 s[36:37], 0x9000
	v_mov_b32_e32 v18, v195
	v_mov_b32_e32 v19, v195
	v_mov_b32_e32 v20, v195
	v_mov_b32_e32 v21, v195
	v_mov_b32_e32 v22, v195
	v_mov_b32_e32 v23, v195
	v_mov_b32_e32 v24, v195
	v_mov_b32_e32 v25, v195
	v_mov_b32_e32 v26, v195
	v_mov_b32_e32 v27, v195
	v_mov_b32_e32 v28, v195
	v_mov_b32_e32 v29, v195
	v_mov_b32_e32 v30, v195
	v_mov_b32_e32 v31, v195
	v_mov_b32_e32 v32, v195
	v_mov_b32_e32 v33, v195
	v_mov_b32_e32 v34, v195
	v_mov_b32_e32 v35, v195
	v_mov_b32_e32 v36, v195
	v_mov_b32_e32 v37, v195
	v_mov_b32_e32 v38, v195
	v_mov_b32_e32 v39, v195
	v_mov_b32_e32 v40, v195
	v_mov_b32_e32 v41, v195
	v_mov_b32_e32 v42, v195
	v_mov_b32_e32 v43, v195
	v_mov_b32_e32 v44, v195
	v_mov_b32_e32 v45, v195
	v_mov_b32_e32 v46, v195
	v_mov_b32_e32 v47, v195
	v_mov_b32_e32 v48, v195
	v_mov_b32_e32 v49, v195

.LBB1_222:
	v_readfirstlane_b32 s16, v0
	s_mov_b32 s23, 0
	s_lshr_b32 s38, s16, 6
	s_lshl_b64 s[0:1], s[22:23], 11
	s_lshl_b32 s39, s33, 18
	s_lshl_b32 s17, s33, 19
	s_add_u32 s8, s8, s17
	s_addc_u32 s9, s9, 0
	s_lshl_b32 s30, s38, 5
	s_add_u32 s0, s30, s0
	s_addc_u32 s1, 0, s1
	s_add_u32 s0, s0, 0x400
	s_addc_u32 s1, s1, 0
	s_lshl_b64 s[6:7], s[0:1], 6
	s_lshl_b64 s[0:1], s[0:1], 7
	s_add_u32 s8, s8, s0
	s_addc_u32 s9, s9, s1
	s_lshr_b32 s0, s16, 4
	s_and_b32 s20, s16, 0x3fffffc0
	s_and_b32 s0, s0, 4
	v_bitop3_b32 v4, s0, v1, v220 bitop3:0x36
	s_add_u32 s0, s10, s17
	s_addc_u32 s1, s11, 0
	s_lshl_b64 s[18:19], s[22:23], 18
	s_add_u32 s0, s0, s18
	v_lshl_or_b32 v194, s38, 3, v199
	v_mov_b32_e32 v195, 0
	s_addc_u32 s1, s1, s19
	v_lshlrev_b64 v[82:83], 7, v[194:195]
	v_lshl_add_u64 v[2:3], s[0:1], 0, v[82:83]
	s_add_u32 s0, s12, s17
	s_addc_u32 s1, s13, 0
	v_lshlrev_b32_e32 v194, 4, v4
	s_add_u32 s0, s0, s18
	v_lshl_add_u64 v[50:51], v[2:3], 0, v[194:195]
	s_addc_u32 s1, s1, s19
	v_lshl_or_b32 v2, s38, 4, v218
	v_mov_b32_e32 v3, v195
	s_lshl_b32 s40, s38, 10
	v_lshlrev_b64 v[84:85], 7, v[2:3]
	s_cmp_lg_u32 0, -1
	v_lshl_add_u64 v[2:3], s[0:1], 0, v[84:85]
	v_and_b32_e32 v42, 24, v219
	s_cselect_b32 s0, 0, 0
	v_lshlrev_b32_e32 v4, 1, v42
	v_mov_b32_e32 v5, v195
	s_add_i32 s40, s40, s0
	s_mov_b32 m0, s40
	s_nop 0
	global_load_lds_dwordx4 v[50:51], off
	s_mov_b64 s[0:1], 0x1000
	v_lshl_add_u64 v[52:53], v[2:3], 0, v[4:5]
	v_lshl_add_u64 v[2:3], v[50:51], 0, s[0:1]
	s_add_i32 s21, s40, 0x1000
	s_mov_b32 m0, s21
	s_nop 0
	global_load_lds_dwordx4 v[2:3], off
	s_add_i32 s41, s40, 0x6000
	s_mov_b32 m0, s41
	s_nop 0
	global_load_lds_dwordx4 v[52:53], off
	s_add_i32 s0, s40, 0x7000
	v_lshl_add_u64 v[2:3], v[52:53], 0, 64
	s_mov_b32 m0, s0
	s_nop 0
	global_load_lds_dwordx4 v[2:3], off
	s_mov_b64 s[0:1], 0x2000
	s_add_i32 s16, s40, 0x2000
	v_lshl_add_u64 v[2:3], v[50:51], 0, s[0:1]
	s_mov_b32 m0, s16
	s_nop 0
	global_load_lds_dwordx4 v[2:3], off
	s_mov_b64 s[16:17], 0x3000
	v_lshlrev_b32_e32 v4, 7, v211
	v_lshl_add_u64 v[2:3], v[50:51], 0, s[16:17]
	s_add_i32 s16, s40, 0x3000
	s_mov_b32 m0, s16
	s_nop 0
	global_load_lds_dwordx4 v[2:3], off
	v_or_b32_e32 v2, v212, v4
	global_load_dwordx4 v[150:153], v2, s[8:9]
	global_load_dwordx4 v[146:149], v2, s[8:9] offset:32
	global_load_dwordx4 v[138:141], v2, s[8:9] offset:64
	global_load_dwordx4 v[122:125], v2, s[8:9] offset:96
	v_bitop3_b32 v3, v210, v217, 7 bitop3:0x78
	v_lshlrev_b32_e32 v209, 4, v3
	v_add_u32_e32 v217, 0, v4
	v_mov_b32_e32 v2, v195
	v_mov_b32_e32 v3, v195
	v_mov_b32_e32 v4, v195
	v_mov_b32_e32 v6, v195
	v_mov_b32_e32 v7, v195
	v_mov_b32_e32 v8, v195
	v_mov_b32_e32 v9, v195
	v_mov_b32_e32 v10, v195
	v_mov_b32_e32 v11, v195
	v_mov_b32_e32 v12, v195
	v_mov_b32_e32 v13, v195
	v_mov_b32_e32 v14, v195
	v_mov_b32_e32 v15, v195
	v_mov_b32_e32 v16, v195
	v_mov_b32_e32 v17, v195
	s_mov_b64 s[8:9], 0x4000
	s_add_i32 s16, s40, 0x4000
	v_lshl_add_u64 v[18:19], v[50:51], 0, s[8:9]
	s_mov_b32 m0, s16
	s_nop 0
	global_load_lds_dwordx4 v[18:19], off
	s_mov_b64 s[16:17], 0x5000
	v_lshl_add_u64 v[18:19], v[50:51], 0, s[16:17]
	s_add_i32 s16, s40, 0x5000
	s_mov_b32 m0, s16
	s_nop 0
	global_load_lds_dwordx4 v[18:19], off
	s_waitcnt vmcnt(6) lgkmcnt(0)
	s_barrier
	v_add_u32_e32 v218, v217, v209
	ds_read_b128 v[34:37], v218
	ds_read_b128 v[38:41], v218 offset:4096
	v_xor_b32_e32 v219, 32, v209
	v_add_u32_e32 v220, v217, v219
	v_xor_b32_e32 v221, 64, v209
	v_add_u32_e32 v222, v217, v221
	v_xor_b32_e32 v223, 0x60, v209
	v_add_u32_e32 v224, v217, v223
	s_mov_b64 s[16:17], 0x6000
	s_mov_b64 s[24:25], 0x7000
	s_waitcnt vmcnt(5) lgkmcnt(0)
	v_mfma_f32_32x32x16_f16 v[18:33], v[34:37], v[150:153], v[2:17]
	s_lshl_b32 s20, s20, 2
	s_lshl_b32 s2, s2, 15
	s_add_i32 s33, s20, 0
	s_lshl_b32 s3, s3, 19
	s_and_b32 s2, s2, 0x400000
	s_mov_b32 s31, -1
	s_movk_i32 s36, 0x2000
	v_mfma_f32_32x32x16_f16 v[2:17], v[38:41], v[150:153], v[2:17]
	ds_read_b128 v[34:37], v220
	ds_read_b128 v[38:41], v220 offset:4096
	s_movk_i32 s34, 0x4000
	s_or_b32 s22, s2, s3
	s_mov_b64 s[2:3], 0x8000
	s_mov_b32 s35, 0x41000000
	s_mov_b32 s26, s23
	v_lshl_add_u32 v207, v211, 2, s33
	s_waitcnt vmcnt(4) lgkmcnt(1)
	v_mfma_f32_32x32x16_f16 v[18:33], v[34:37], v[146:149], v[18:33]
	s_waitcnt lgkmcnt(0)
	v_mfma_f32_32x32x16_f16 v[2:17], v[38:41], v[146:149], v[2:17]
	ds_read_b128 v[34:37], v222
	ds_read_b128 v[38:41], v222 offset:4096
	s_waitcnt vmcnt(3) lgkmcnt(1)
	v_mfma_f32_32x32x16_f16 v[18:33], v[34:37], v[138:141], v[18:33]
	s_waitcnt lgkmcnt(0)
	v_mfma_f32_32x32x16_f16 v[2:17], v[38:41], v[138:141], v[2:17]
	ds_read_b128 v[34:37], v224
	ds_read_b128 v[38:41], v224 offset:4096
	s_waitcnt vmcnt(0) lgkmcnt(1)
	v_mfma_f32_32x32x16_f16 v[18:33], v[34:37], v[122:125], v[18:33]
	s_waitcnt lgkmcnt(0)
	v_mfma_f32_32x32x16_f16 v[2:17], v[38:41], v[122:125], v[2:17]
	s_nop 9
	v_max_f32_e32 v34, v19, v19
	v_max_f32_e32 v35, v18, v18
	v_max_f32_e32 v34, v35, v34
	v_max3_f32 v36, v20, v21, v3
	v_max3_f32 v34, v34, v2, v4
	v_max3_f32 v35, v36, v24, v25
	v_max3_f32 v34, v34, v5, v22
	v_max3_f32 v35, v35, v8, v9
	v_max3_f32 v34, v34, v23, v6
	v_max3_f32 v35, v35, v28, v29
	v_max3_f32 v34, v34, v7, v26
	v_max3_f32 v35, v35, v12, v13
	v_max3_f32 v34, v34, v27, v10
	v_max3_f32 v35, v35, v32, v33
	v_max3_f32 v34, v34, v11, v30
	v_max3_f32 v35, v35, v16, v17
	v_max3_f32 v34, v34, v31, v14
	v_max3_f32 v34, v34, v15, v35
	v_mov_b32_e32 v35, v34
	s_nop 1
	v_permlane32_swap_b32_e32 v34, v35
	v_max_f32_e32 v35, v35, v35
	v_max_f32_e32 v34, v34, v34
	v_max_f32_e32 v208, v34, v35
	v_sub_f32_e32 v54, v2, v208
	v_and_b32_e32 v2, 32, v215
	v_xor_b32_e32 v34, 0x80000000, v208
	v_add3_u32 v2, 0, v2, v42
	v_mov_b32_e32 v35, v34
	v_mov_b32_e32 v36, v34
	v_mov_b32_e32 v37, v34
	v_mov_b32_e32 v38, v34
	v_mov_b32_e32 v39, v34
	v_mov_b32_e32 v40, v34
	v_mov_b32_e32 v41, v34
	v_mov_b32_e32 v42, v34
	v_mov_b32_e32 v43, v34
	v_mov_b32_e32 v44, v34
	v_mov_b32_e32 v45, v34
	v_mov_b32_e32 v46, v34
	v_mov_b32_e32 v47, v34
	v_mov_b32_e32 v48, v34
	v_mov_b32_e32 v49, v34
	v_sub_f32_e32 v55, v3, v208
	v_and_b32_e32 v3, 0xc0, v216
	s_waitcnt vmcnt(0) lgkmcnt(0)
	s_barrier
	v_add3_u32 v206, v2, v214, v3
	v_lshl_add_u64 v[2:3], v[50:51], 0, s[16:17]
	s_mov_b32 m0, s40
	s_nop 0
	global_load_lds_dwordx4 v[2:3], off
	v_lshl_add_u64 v[2:3], v[50:51], 0, s[24:25]
	s_mov_b32 m0, s21
	s_nop 0
	global_load_lds_dwordx4 v[2:3], off
	s_add_i32 s21, s40, 0x8000
	v_lshl_add_u64 v[2:3], v[52:53], 0, s[0:1]
	s_mov_b32 m0, s21
	s_nop 0
	global_load_lds_dwordx4 v[2:3], off
	s_mov_b64 s[0:1], 0x2040
	v_lshl_add_u64 v[2:3], v[52:53], 0, s[0:1]
	s_add_i32 s0, s40, 0x9000
	s_mov_b32 m0, s0
	s_nop 0
	global_load_lds_dwordx4 v[2:3], off
	ds_read_b128 v[182:185], v218 offset:8192
	ds_read_b128 v[178:181], v218 offset:12288
	ds_read_b128 v[174:177], v220 offset:8192
	ds_read_b128 v[170:173], v220 offset:12288
	ds_read_b128 v[166:169], v222 offset:8192
	ds_read_b128 v[162:165], v222 offset:12288
	ds_read_b128 v[158:161], v224 offset:8192
	ds_read_b128 v[154:157], v224 offset:12288
	v_lshl_add_u64 v[2:3], s[18:19], 0, v[84:85]
	v_sub_f32_e32 v18, v18, v208
	v_sub_f32_e32 v19, v19, v208
	v_sub_f32_e32 v20, v20, v208
	v_sub_f32_e32 v21, v21, v208
	v_sub_f32_e32 v22, v22, v208
	v_sub_f32_e32 v23, v23, v208
	v_sub_f32_e32 v24, v24, v208
	v_sub_f32_e32 v25, v25, v208
	v_sub_f32_e32 v26, v26, v208
	v_sub_f32_e32 v27, v27, v208
	v_sub_f32_e32 v28, v28, v208
	v_sub_f32_e32 v29, v29, v208
	v_sub_f32_e32 v30, v30, v208
	v_sub_f32_e32 v31, v31, v208
	v_sub_f32_e32 v32, v32, v208
	v_sub_f32_e32 v33, v33, v208
	v_sub_f32_e32 v4, v4, v208
	v_sub_f32_e32 v5, v5, v208
	v_sub_f32_e32 v6, v6, v208
	v_sub_f32_e32 v7, v7, v208
	v_sub_f32_e32 v8, v8, v208
	v_sub_f32_e32 v9, v9, v208
	v_sub_f32_e32 v10, v10, v208
	v_sub_f32_e32 v11, v11, v208
	v_sub_f32_e32 v12, v12, v208
	v_sub_f32_e32 v13, v13, v208
	v_sub_f32_e32 v14, v14, v208
	v_sub_f32_e32 v15, v15, v208
	v_sub_f32_e32 v16, v16, v208
	v_sub_f32_e32 v17, v17, v208
	v_lshl_or_b32 v2, v213, 4, v2
	v_exp_f32_e32 v66, v18
	v_exp_f32_e32 v67, v19
	v_exp_f32_e32 v50, v54
	v_exp_f32_e32 v51, v55
	v_exp_f32_e32 v68, v20
	v_exp_f32_e32 v52, v4
	v_exp_f32_e32 v69, v21
	v_exp_f32_e32 v53, v5
	v_exp_f32_e32 v70, v22
	v_exp_f32_e32 v54, v6
	v_exp_f32_e32 v71, v23
	v_exp_f32_e32 v55, v7
	v_exp_f32_e32 v72, v24
	v_exp_f32_e32 v56, v8
	v_exp_f32_e32 v73, v25
	v_exp_f32_e32 v57, v9
	v_exp_f32_e32 v74, v26
	v_exp_f32_e32 v58, v10
	v_exp_f32_e32 v75, v27
	v_exp_f32_e32 v59, v11
	v_exp_f32_e32 v76, v28
	v_exp_f32_e32 v60, v12
	v_exp_f32_e32 v77, v29
	v_exp_f32_e32 v61, v13
	v_exp_f32_e32 v78, v30
	v_exp_f32_e32 v62, v14
	v_exp_f32_e32 v79, v31
	v_exp_f32_e32 v63, v15
	v_exp_f32_e32 v80, v32
	v_exp_f32_e32 v64, v16
	v_exp_f32_e32 v81, v33
	v_exp_f32_e32 v65, v17
	v_lshl_add_u64 v[190:191], s[12:13], 0, v[2:3]
	v_lshl_add_u64 v[2:3], s[18:19], 0, v[82:83]
	s_waitcnt vmcnt(4) lgkmcnt(0)
	s_barrier
	v_or_b32_e32 v2, v2, v194
	v_lshl_add_u64 v[192:193], s[10:11], 0, v[2:3]
	v_cmp_gt_u32_e64 s[0:1], 32, v201
	s_mov_b64 s[10:11], 0x9000
	s_mov_b64 s[12:13], 0x4040
	s_mov_b64 s[18:19], 0xa000
	s_mov_b64 s[20:21], 0xb000
	s_mov_b64 s[24:25], 0x6040
	v_mov_b32_e32 v2, v195
	v_mov_b32_e32 v3, v195
	v_mov_b32_e32 v4, v195
	v_mov_b32_e32 v5, v195
	v_mov_b32_e32 v6, v195
	v_mov_b32_e32 v7, v195
	v_mov_b32_e32 v8, v195
	v_mov_b32_e32 v9, v195
	v_mov_b32_e32 v10, v195
	v_mov_b32_e32 v11, v195
	v_mov_b32_e32 v12, v195
	v_mov_b32_e32 v13, v195
	v_mov_b32_e32 v14, v195
	v_mov_b32_e32 v15, v195
	v_mov_b32_e32 v16, v195
	v_mov_b32_e32 v17, v195
	v_mov_b32_e32 v18, v195
	v_mov_b32_e32 v19, v195
	v_mov_b32_e32 v20, v195
	v_mov_b32_e32 v21, v195
	v_mov_b32_e32 v22, v195
	v_mov_b32_e32 v23, v195
	v_mov_b32_e32 v24, v195
	v_mov_b32_e32 v25, v195
	v_mov_b32_e32 v26, v195
	v_mov_b32_e32 v27, v195
	v_mov_b32_e32 v28, v195
	v_mov_b32_e32 v29, v195
	v_mov_b32_e32 v30, v195
	v_mov_b32_e32 v31, v195
	v_mov_b32_e32 v32, v195
	v_mov_b32_e32 v33, v195
	v_mov_b64_e32 v[196:197], v[192:193]
	v_mov_b64_e32 v[200:201], v[190:191]
